# v39 with the P2 background copy split evenly over all workgroups (no extra tail for the 9-unit workgroups)
# baseline (speedup 1.0000x reference)
.LBB0_376:
	s_andn2_b64 vcc, exec, s[8:9]
	s_cbranch_vccnz .LBB0_599
	s_cmpk_eq_i32 s52, 0x100
	s_cselect_b64 s[0:1], -1, 0
	s_mov_b32 s10, 0x8200
	s_and_b64 s[8:9], s[0:1], exec
	s_cselect_b32 s21, s10, 0x8200
	s_lshl_b32 s8, s86, 3
	s_add_i32 s57, s8, s88
	s_mul_i32 s8, s88, 0x4100
	s_add_i32 s20, s8, 0
	s_cmp_ge_i32 s57, s21
	s_waitcnt vmcnt(0)
	s_barrier
	s_cbranch_scc1 .LBB0_486
	s_ashr_i32 s8, s57, 9
	s_mulk_i32 s8, 0x300
	s_and_b32 s16, s57, 0x1ff
	s_add_i32 s17, s8, s16
	s_addk_i32 s17, 0x3000
	s_cmpk_gt_i32 s17, 0x25ff
	s_cbranch_scc0 .LBB0_385
	s_cmpk_gt_u32 s17, 0x27ff
	s_cbranch_scc0 .LBB0_386
	s_cmpk_gt_u32 s17, 0x2bff
	s_cbranch_scc0 .LBB0_387
	s_cmpk_gt_u32 s17, 0x2fff
	s_cbranch_scc0 .LBB0_388
	s_add_i32 s18, s17, 0xffffd000
	s_and_b32 s8, s18, 0xffff
	s_mul_i32 s8, s8, 0xaaab
	s_lshr_b32 s14, s8, 25
	s_mul_i32 s8, s14, 0x300
	s_sub_i32 s8, s18, s8
	s_and_b32 s15, s8, 0xffff
	s_cmpk_gt_u32 s15, 0x1ff
	s_cbranch_scc0 .LBB0_389
	s_cmpk_gt_u32 s18, 0xbfff
	s_cbranch_scc0 .LBB0_390
	s_add_i32 s8, 0, 0x27ea8
	v_mov_b32_e32 v2, s8
	ds_read_b64 v[2:3], v2
	s_mov_b64 s[10:11], 0
	s_waitcnt lgkmcnt(0)
	v_readfirstlane_b32 s8, v2
	v_readfirstlane_b32 s9, v3
	s_branch .LBB0_391

.LBB0_486:
	s_cmpk_lt_i32 s90, 0x80
	s_cselect_b64 s[8:9], -1, 0
	s_xor_b64 s[0:1], s[0:1], -1
	s_or_b64 s[0:1], s[8:9], s[0:1]
	s_and_b64 vcc, exec, s[0:1]
	s_cbranch_vccnz .LBB0_598
	s_lshl_b32 s14, s90, 3
	s_add_i32 s14, s14, s88
	s_add_i32 s17, s14, 0xfffffc00
	s_cmp_gt_i32 s17, -1
	s_cbranch_scc1 .LBB0_598
	s_add_i32 s0, s17, 0x7800
	s_ashr_i32 s0, s0, 9
	s_and_b32 s15, s17, 0x1ff
	s_mul_i32 s16, s0, 0x300
	s_or_b32 s18, s15, 0x3000
	s_add_i32 s16, s16, s18
	s_cmpk_gt_i32 s16, 0x25ff
	s_cbranch_scc0 .LBB0_495
	s_cmpk_gt_u32 s16, 0x27ff
	s_cbranch_scc0 .LBB0_496
	s_cmpk_gt_u32 s16, 0x2bff
	s_cbranch_scc0 .LBB0_497
	s_cmpk_gt_u32 s16, 0x2fff
	s_cbranch_scc0 .LBB0_498
	s_add_i32 s19, s16, 0xffffd000
	s_and_b32 s0, s19, 0xffff
	s_mul_i32 s0, s0, 0xaaab
	s_lshr_b32 s12, s0, 25
	s_mul_i32 s0, s12, 0x300
	s_sub_i32 s0, s19, s0
	s_and_b32 s13, s0, 0xffff
	s_cmpk_gt_u32 s13, 0x1ff
	s_cbranch_scc0 .LBB0_499
	s_cmpk_gt_u32 s19, 0xbfff
	s_cbranch_scc0 .LBB0_500
	s_add_i32 s0, 0, 0x27ea8
	s_waitcnt vmcnt(15)
	v_mov_b32_e32 v2, s0
	ds_read_b64 v[2:3], v2
	s_mov_b64 s[8:9], 0
	s_waitcnt lgkmcnt(0)
	v_readfirstlane_b32 s0, v2
	v_readfirstlane_b32 s1, v3
	s_branch .LBB0_501
